# baseline (speedup 1.0000x reference)
.LBB0_86:
	s_or_b64 exec, exec, s[0:1]
	v_cmp_ne_u32_e32 vcc, 0, v14
	s_waitcnt lgkmcnt(0)
	s_barrier
	s_setprio 2
	v_and_b32_e32 v40, 15, v1
	v_lshrrev_b32_e32 v41, 4, v1
	s_and_b32 s44, s36, 1
	s_lshr_b32 s45, s36, 1
	s_mov_b32 s60, 0xffff
	s_mov_b32 s61, 0
	s_mov_b32 s62, 0xffff0000
	s_mov_b32 s63, 0
	s_mov_b32 s64, 0
	s_mov_b32 s65, 0xffff
	s_mov_b32 s66, 0
	s_mov_b32 s67, 0xffff0000
	v_cvt_pk_f16_f32 v2, v152, v153
	v_cvt_pk_f16_f32 v3, v154, v155
	v_cvt_pk_f16_f32 v4, v156, v157
	v_cvt_pk_f16_f32 v5, v158, v159
	s_lshl_b32 s46, s44, 3
	v_lshl_add_u32 v42, v41, 1, s46
	v_mul_u32_u24_e32 v32, 0x650, v42
	v_lshl_add_u32 v34, v40, 3, v32
	v_mul_u32_u24_e32 v33, 0x650, v40
	v_add_u32_e32 v33, 0x6500, v33
	s_lshl_b32 s47, s45, 1
	s_lshl_b32 s46, s44, 10
	s_add_i32 s47, s47, s46
	s_add_i32 s47, s47, 0xca00
	v_lshl_add_u32 v39, v40, 2, s47
	v_lshl_add_u32 v39, v41, 8, v39
	v_lshlrev_b32_e32 v43, 4, v1
	v_add_u32_e32 v43, 0xca00, v43
	v_lshlrev_b32_e32 v35, 4, v1
	v_mov_b32_e32 v44, 1
	s_lshl_b32 s46, s3, 2
	s_add_i32 s46, s46, s33
	s_mul_i32 s46, s46, 0x3200
	s_add_u32 s68, s26, s46
	s_addc_u32 s69, s27, 0
	s_mov_b32 s73, 0
	v_mov_b32_e32 v36, 0x14a00

	.amdhsa_kernel _Z2kA5AArgs
		.amdhsa_group_segment_fixed_size 84672
		.amdhsa_private_segment_fixed_size 0
		.amdhsa_kernarg_size 120
		.amdhsa_user_sgpr_count 2
		.amdhsa_user_sgpr_dispatch_ptr 0
		.amdhsa_user_sgpr_queue_ptr 0
		.amdhsa_user_sgpr_kernarg_segment_ptr 1
		.amdhsa_user_sgpr_dispatch_id 0
		.amdhsa_user_sgpr_kernarg_preload_length 0
		.amdhsa_user_sgpr_kernarg_preload_offset 0
		.amdhsa_user_sgpr_private_segment_size 0
		.amdhsa_uses_dynamic_stack 0
		.amdhsa_enable_private_segment 0
		.amdhsa_system_sgpr_workgroup_id_x 1
		.amdhsa_system_sgpr_workgroup_id_y 0
		.amdhsa_system_sgpr_workgroup_id_z 0
		.amdhsa_system_sgpr_workgroup_info 0
		.amdhsa_system_vgpr_workitem_id 0
		.amdhsa_next_free_vgpr 224
		.amdhsa_next_free_sgpr 96
		.amdhsa_accum_offset 224
		.amdhsa_reserve_vcc 1
		.amdhsa_float_round_mode_32 0
		.amdhsa_float_round_mode_16_64 0
		.amdhsa_float_denorm_mode_32 3
		.amdhsa_float_denorm_mode_16_64 3
		.amdhsa_dx10_clamp 1
		.amdhsa_ieee_mode 1
		.amdhsa_fp16_overflow 0
		.amdhsa_tg_split 0
		.amdhsa_exception_fp_ieee_invalid_op 0
		.amdhsa_exception_fp_denorm_src 0
		.amdhsa_exception_fp_ieee_div_zero 0
		.amdhsa_exception_fp_ieee_overflow 0
		.amdhsa_exception_fp_ieee_underflow 0
		.amdhsa_exception_fp_ieee_inexact 0
		.amdhsa_exception_int_div_zero 0
	.end_amdhsa_kernel

amdhsa.kernels:
  - .agpr_count:     0
    .args:
      - .offset:         0
        .size:           120
        .value_kind:     by_value
    .group_segment_fixed_size: 84672
    .kernarg_segment_align: 8
    .kernarg_segment_size: 120
    .language:       OpenCL C
    .language_version:
      - 2
      - 0
    .max_flat_workgroup_size: 512
    .name:           _Z2kA5AArgs
    .private_segment_fixed_size: 0
    .sgpr_count:     50
    .sgpr_spill_count: 0
    .symbol:         _Z2kA5AArgs.kd
    .uniform_work_group_size: 1
    .uses_dynamic_stack: false
    .vgpr_count:     224
    .vgpr_spill_count: 0
    .wavefront_size: 64
  - .agpr_count:     0
    .args:
      - .actual_access:  read_only
        .address_space:  global
        .offset:         0
        .size:           8
        .value_kind:     global_buffer
      - .actual_access:  read_only
        .address_space:  global
        .offset:         8
        .size:           8
        .value_kind:     global_buffer
      - .actual_access:  read_only
        .address_space:  global
        .offset:         16
        .size:           8
        .value_kind:     global_buffer
      - .actual_access:  read_only
        .address_space:  global
        .offset:         24
        .size:           8
        .value_kind:     global_buffer
      - .actual_access:  read_only
        .address_space:  global
        .offset:         32
        .size:           8
        .value_kind:     global_buffer
      - .actual_access:  read_only
        .address_space:  global
        .offset:         40
        .size:           8
        .value_kind:     global_buffer
      - .actual_access:  write_only
        .address_space:  global
        .offset:         48
        .size:           8
        .value_kind:     global_buffer
    .group_segment_fixed_size: 65792
    .kernarg_segment_align: 8
    .kernarg_segment_size: 56
    .language:       OpenCL C
    .language_version:
      - 2
      - 0
    .max_flat_workgroup_size: 512
    .name:           _Z2kBPKfPKDv4_jPKDF16_S0_S0_S0_Pf
    .private_segment_fixed_size: 0
    .sgpr_count:     18
    .sgpr_spill_count: 0
    .symbol:         _Z2kBPKfPKDv4_jPKDF16_S0_S0_S0_Pf.kd
    .uniform_work_group_size: 1
    .uses_dynamic_stack: false
    .vgpr_count:     109
    .vgpr_spill_count: 0
    .wavefront_size: 64
